# E prologue: the 16-entry tile prefix sum formed in registers (readlane/writelane + scalar running sum) instead of a 16-step dependent LDS chain on thread 0
# speedup vs baseline: 1.0025x; 1.0025x over previous
.LBB0_1032:
	s_mov_b32 s0, s47
	v_mbcnt_lo_u32_b32 v1, -1, 0
	v_mbcnt_hi_u32_b32 v1, -1, v1
	s_mov_b32 s59, s68
	v_lshl_add_u32 v1, s0, 6, v1
	s_mov_b32 s2, s73
	s_mov_b32 s0, s69
	s_movk_i32 s3, 0x2000
	ds_read_b32 v2, v0 offset:704
	ds_read_b32 v3, v0 offset:708
	v_cmp_gt_i32_e32 vcc, 16, v1
	s_waitcnt lgkmcnt(0)
	v_readfirstlane_b32 s6, v2
	ds_read_b32 v2, v0 offset:696
	s_waitcnt lgkmcnt(0)
	ds_read_b32 v2, v0 offset:700
	v_readfirstlane_b32 s7, v3
	s_and_saveexec_b64 s[0:1], vcc
	s_cbranch_execz .LBB0_1034
	v_readlane_b32 s4, v255, 19
	s_waitcnt lgkmcnt(0)
	s_nop 0
	v_lshl_add_u32 v2, v1, 6, s4
	v_ashrrev_i32_e32 v3, 31, v2
	v_lshl_add_u64 v[2:3], v[2:3], 2, s[6:7]
	v_add_co_u32_e32 v2, vcc, 0x10000, v2
	s_nop 1
	v_addc_co_u32_e32 v3, vcc, 0, v3, vcc
	global_load_dword v2, v[2:3], off sc1
	v_lshl_add_u32 v3, v1, 2, 0
	s_waitcnt vmcnt(0)
	ds_write_b32 v3, v2 offset:160
	v_add_u32_e32 v2, 0xff, v2
	v_ashrrev_i32_e32 v2, 8, v2
	s_mov_b32 s4, 0
	v_readlane_b32 s5, v2, 0
	v_writelane_b32 v4, s4, 0
	s_add_i32 s4, s4, s5
	v_readlane_b32 s5, v2, 1
	v_writelane_b32 v4, s4, 1
	s_add_i32 s4, s4, s5
	v_readlane_b32 s5, v2, 2
	v_writelane_b32 v4, s4, 2
	s_add_i32 s4, s4, s5
	v_readlane_b32 s5, v2, 3
	v_writelane_b32 v4, s4, 3
	s_add_i32 s4, s4, s5
	v_readlane_b32 s5, v2, 4
	v_writelane_b32 v4, s4, 4
	s_add_i32 s4, s4, s5
	v_readlane_b32 s5, v2, 5
	v_writelane_b32 v4, s4, 5
	s_add_i32 s4, s4, s5
	v_readlane_b32 s5, v2, 6
	v_writelane_b32 v4, s4, 6
	s_add_i32 s4, s4, s5
	v_readlane_b32 s5, v2, 7
	v_writelane_b32 v4, s4, 7
	s_add_i32 s4, s4, s5
	v_readlane_b32 s5, v2, 8
	v_writelane_b32 v4, s4, 8
	s_add_i32 s4, s4, s5
	v_readlane_b32 s5, v2, 9
	v_writelane_b32 v4, s4, 9
	s_add_i32 s4, s4, s5
	v_readlane_b32 s5, v2, 10
	v_writelane_b32 v4, s4, 10
	s_add_i32 s4, s4, s5
	v_readlane_b32 s5, v2, 11
	v_writelane_b32 v4, s4, 11
	s_add_i32 s4, s4, s5
	v_readlane_b32 s5, v2, 12
	v_writelane_b32 v4, s4, 12
	s_add_i32 s4, s4, s5
	v_readlane_b32 s5, v2, 13
	v_writelane_b32 v4, s4, 13
	s_add_i32 s4, s4, s5
	v_readlane_b32 s5, v2, 14
	v_writelane_b32 v4, s4, 14
	s_add_i32 s4, s4, s5
	v_readlane_b32 s5, v2, 15
	v_writelane_b32 v4, s4, 15
	s_add_i32 s4, s4, s5
	ds_write_b32 v3, v4 offset:64
	v_mov_b32_e32 v5, s4
	ds_write_b32 v0, v5 offset:128
.LBB0_1034:
	s_or_b64 exec, exec, s[0:1]
	v_cmp_eq_u32_e32 vcc, 0, v1
	s_waitcnt lgkmcnt(0)
	s_barrier
	s_and_saveexec_b64 s[0:1], vcc
	s_cbranch_execz .LBB0_1036
.LBB0_1036:
	s_or_b64 exec, exec, s[0:1]
	s_add_i32 s3, s3, 0
	s_add_u32 s82, s6, 0x400000
	s_addc_u32 s83, s7, 0
	s_add_u32 s84, s6, 0x1c600000
	s_addc_u32 s85, s7, 0
	s_add_u32 s4, s6, s80
	s_addc_u32 s5, s7, s81
	s_lshl_b32 s24, s58, 17
	s_lshl_b64 s[0:1], s[24:25], 2
	s_add_u32 s0, s4, s0
	s_mov_b32 s4, s47
	s_waitcnt lgkmcnt(0)
	s_barrier
	v_mbcnt_lo_u32_b32 v4, -1, 0
	v_mbcnt_hi_u32_b32 v4, -1, v4
	ds_read_b32 v2, v0 offset:128
	s_addc_u32 s1, s5, s1
	s_add_u32 s65, s0, 0x20000
	s_addc_u32 s66, s1, 0
	v_lshl_add_u32 v1, s4, 6, v4
	s_waitcnt lgkmcnt(0)
	v_readfirstlane_b32 s0, v2
	s_mul_i32 s0, s0, 6
	s_cmp_ge_i32 s2, s0
	v_readfirstlane_b32 s4, v1
	s_cbranch_scc1 .LBB0_1074
	s_and_b32 s1, s59, 7
	s_cmp_eq_u32 s1, 0
	s_cselect_b64 s[8:9], -1, 0
	s_cmp_lg_u32 s1, 0
	s_mov_b32 s14, s2
	s_cbranch_scc1 .LBB0_1043
	s_ashr_i32 s12, s0, 3
	s_and_b32 s13, s0, 6
	s_and_b32 s5, s2, 7
	s_add_i32 s10, s12, 1
	s_cmp_ge_u32 s5, s13
	s_mov_b64 s[0:1], -1
	s_cbranch_scc0 .LBB0_1040
	s_sub_i32 s1, s5, s13
	s_mul_i32 s0, s10, s13
	s_mul_i32 s1, s1, s12
	s_add_i32 s11, s0, s1
	s_mov_b64 s[0:1], 0
